# rope loop: all 20 ushort loads + V load prefetched one token ahead, wave_sum via DPP (quad_perm/row_mirror/row_bcast) batched over 10 heads instead of serial ds_bpermute
# speedup vs baseline: 1.0330x; 1.0123x over previous
; __device__ __forceinline__ float bf2f(bf16_t b) { return __uint_as_float((unsigned)b << 16); }
; __device__ __forceinline__ bf16_t f2bf(float f) { return (bf16_t)(cvt_pk_bf16(f, 0.f) & 0xffffu); }
; __device__ __forceinline__ void rope_token(const bf16_t* __restrict__ proj, const float* __restrict__ qg, const float* __restrict__ kg, bf16_t* __restrict__ QN, bf16_t* __restrict__ KN, bf16_t* __restrict__ VN, int tok, int lane) {
;     const int a = lane >> 5, f = lane & 31, i1 = a * 64 + f, i2 = i1 + 32; const int t = tok & (SEQ - 1);
;     const float pos = a == 0 ? (float)((t >> 6) - 32) : (float)((t & 63) - 32);
;     const float inv = exp2f(-(float)f * (13.287712379549449f / 32.f)); float sn, cs; sincosf(pos * inv, &sn, &cs);
;     const bf16_t* src = proj + (size_t)tok * NIN;
; #pragma unroll
;     for (int hh = 0; hh < 10; ++hh) { const bf16_t* s = src + hh * 128; float x1 = bf2f(s[i1]), x2 = bf2f(s[i2]);
;         const float ss = wave_sum(x1 * x1 + x2 * x2), rs = rsqrtf(ss * (1.f / 128.f) + EPS); const float* gn = hh < 8 ? qg : kg;
;         x1 *= rs * gn[i1]; x2 *= rs * gn[i2];
;         bf16_t* d = hh < 8 ? QN + (size_t)tok * 1024 + hh * 128 : KN + (size_t)tok * 256 + (hh - 8) * 128;
;         d[i1] = f2bf(x1 * cs - x2 * sn); d[i2] = f2bf(x2 * cs + x1 * sn); }
;     *(u32x2*)(VN + (size_t)tok * 256 + lane * 4) = *(const u32x2*)(src + C_V + lane * 4);
; }
; __global__ void __launch_bounds__(NWAVES * 64, 2) mk_fwd(Args a) {
;     ...
;         { for (int tok = gw; tok < NT; tok += ngw) thin::rope_token(PROJ, a.in[4] + l * 128, a.in[5] + l * 128, QN, KN, VN, tok, lane);
.LBB0_582:
	s_cmpk_gt_i32 s96, 0x1fff
	s_cbranch_scc1 .LBB0_595
	v_and_b32_e32 v133, 31, v0
	s_waitcnt vmcnt(0)
	v_cvt_f32_ubyte0_e32 v2, v133
	s_waitcnt lgkmcnt(0)
	v_mul_f32_e32 v3, 0xbed49a78, v2
	s_mov_b32 s0, 0xc2fc0000
	v_mov_b32_e32 v4, 0x42800000
	v_cmp_gt_f32_e64 s[0:1], s0, v3
	v_not_b32_e32 v20, 63
	v_readlane_b32 s36, v247, 3
	v_cndmask_b32_e64 v3, 0, v4, s[0:1]
	v_fmac_f32_e32 v3, 0xbed49a78, v2
	v_exp_f32_e32 v2, v3
	v_cndmask_b32_e64 v3, 0, v20, s[0:1]
	v_readlane_b32 s44, v247, 11
	v_readlane_b32 s45, v247, 12
	v_ldexp_f32 v21, v2, v3
	v_lshlrev_b32_e32 v2, 1, v0
	v_and_or_b32 v6, v2, 64, v133
	v_lshlrev_b32_e32 v2, 2, v6
	s_nop 0
	global_load_dword v22, v2, s[44:45]
	global_load_dword v23, v2, s[44:45] offset:128
	v_mbcnt_lo_u32_b32 v3, -1, 0
	v_mbcnt_hi_u32_b32 v3, -1, v3
	v_and_b32_e32 v4, 64, v3
	v_add_u32_e32 v4, 64, v4
	v_xor_b32_e32 v5, 1, v3
	v_cmp_lt_i32_e64 s[0:1], v5, v4
	v_readlane_b32 s46, v247, 13
	v_readlane_b32 s47, v247, 14
	v_cndmask_b32_e64 v5, v3, v5, s[0:1]
	v_lshlrev_b32_e32 v24, 2, v5
	v_xor_b32_e32 v5, 2, v3
	v_cmp_lt_i32_e64 s[0:1], v5, v4
	s_ashr_i32 s97, s96, 31
	v_lshlrev_b32_e32 v12, 3, v194
	v_cndmask_b32_e64 v5, v3, v5, s[0:1]
	v_lshlrev_b32_e32 v25, 2, v5
	v_xor_b32_e32 v5, 4, v3
	v_cmp_lt_i32_e64 s[0:1], v5, v4
	s_mul_i32 s4, s96, 0x5400
	v_readlane_b32 s37, v247, 4
	v_cndmask_b32_e64 v5, v3, v5, s[0:1]
	v_lshlrev_b32_e32 v26, 2, v5
	v_xor_b32_e32 v5, 8, v3
	v_cmp_lt_i32_e64 s[0:1], v5, v4
	v_readlane_b32 s38, v247, 5
	v_readlane_b32 s39, v247, 6
	v_cndmask_b32_e64 v5, v3, v5, s[0:1]
	v_lshlrev_b32_e32 v27, 2, v5
	v_xor_b32_e32 v5, 16, v3
	v_cmp_lt_i32_e64 s[0:1], v5, v4
	v_readlane_b32 s40, v247, 7
	v_readlane_b32 s41, v247, 8
	v_cndmask_b32_e64 v5, v3, v5, s[0:1]
	v_lshlrev_b32_e32 v28, 2, v5
	v_xor_b32_e32 v5, 32, v3
	v_cmp_lt_i32_e64 s[0:1], v5, v4
	v_readlane_b32 s42, v247, 9
	v_readlane_b32 s43, v247, 10
	v_cndmask_b32_e64 v3, v3, v5, s[0:1]
	v_lshlrev_b32_e32 v29, 2, v3
	v_mov_b32_e32 v3, 0
	v_lshl_add_u64 v[4:5], s[46:47], 0, v[2:3]
	s_lshl_b64 s[0:1], s[96:97], 11
	v_lshlrev_b32_e32 v2, 1, v6
	v_or_b32_e32 v6, s0, v2
	v_mov_b32_e32 v7, s1
	s_lshl_b64 s[0:1], s[96:97], 9
	v_or_b32_e32 v8, s0, v2
	v_mov_b32_e32 v9, s1
	v_or_b32_e32 v10, s0, v12
	v_mov_b32_e32 v11, s1
	s_mov_b64 s[0:1], 0x4e200000
	v_lshl_add_u64 v[10:11], v[10:11], 0, s[0:1]
	s_mul_hi_i32 s0, s96, 0x5400
	s_ashr_i32 s59, s58, 31
	v_or_b32_e32 v12, s4, v12
	v_mov_b32_e32 v13, s0
	s_mov_b64 s[0:1], 0x42600a00
	v_cmp_gt_u32_e32 vcc, 32, v194
	s_lshl_b64 s[14:15], s[58:59], 11
	s_lshl_b64 s[16:17], s[58:59], 9
	v_lshl_add_u64 v[14:15], v[12:13], 0, s[0:1]
	s_mul_hi_i32 s23, s58, 0x5400
	s_mul_i32 s22, s58, 0x5400
	v_or_b32_e32 v12, s4, v2
	s_brev_b32 s20, 18
	s_mov_b32 s21, 0x800000
	s_mov_b32 s28, 0xfe5163ab
	s_mov_b32 s29, 0x3c439041
	s_mov_b32 s30, 0xdb629599
	s_mov_b32 s31, 0xf534ddc0
	s_mov_b32 s35, 0xfc2757d1
	s_mov_b32 s36, 0x4e441529
	s_mov_b32 s37, 0xa2f9836e
	s_mov_b32 s38, 0x3fc90fda
	s_mov_b32 s39, 0x3f22f983
	s_mov_b32 s40, 0xbfc90fda
	v_mov_b32_e32 v30, 0x3c0881c4
	v_mov_b32_e32 v31, 0xbab64f3b
	s_brev_b32 s41, 1
	s_movk_i32 s42, 0x1f8
	s_mov_b32 s43, 0x42600000
	v_mov_b32_e32 v32, 0x358637bd
	s_mov_b32 s44, 0x4ce00000
	s_mov_b32 s45, 0x4de00000
	v_not_b32_e32 v33, 31
	v_mov_b32_e32 v34, 0x7fc00000
	s_mov_b32 s46, s96
	v_readlane_b32 s48, v247, 15
	v_readlane_b32 s49, v247, 16
	v_readlane_b32 s50, v247, 17
	v_readlane_b32 s51, v247, 18
	v_lshl_add_u64 v[222:223], s[52:53], 0, v[12:13]
	v_lshl_add_u64 v[224:225], s[52:53], 0, v[14:15]
	v_mov_b32_e32 v192, 0x3c000000
	v_add_co_u32_e64 v222, s[0:1], s43, v222
	s_nop 1
	v_addc_co_u32_e64 v223, s[0:1], 0, v223, s[0:1]
	global_load_dword v190, v[4:5], off
	global_load_dword v191, v[4:5], off offset:128
	global_load_ushort v200, v[222:223], off
	global_load_ushort v201, v[222:223], off offset:64
	global_load_ushort v202, v[222:223], off offset:256
	global_load_ushort v203, v[222:223], off offset:320
	global_load_ushort v204, v[222:223], off offset:512
	global_load_ushort v205, v[222:223], off offset:576
	global_load_ushort v206, v[222:223], off offset:768
	global_load_ushort v207, v[222:223], off offset:832
	global_load_ushort v208, v[222:223], off offset:1024
	global_load_ushort v209, v[222:223], off offset:1088
	global_load_ushort v210, v[222:223], off offset:1280
	global_load_ushort v211, v[222:223], off offset:1344
	global_load_ushort v212, v[222:223], off offset:1536
	global_load_ushort v213, v[222:223], off offset:1600
	global_load_ushort v214, v[222:223], off offset:1792
	global_load_ushort v215, v[222:223], off offset:1856
	global_load_ushort v216, v[222:223], off offset:2048
	global_load_ushort v217, v[222:223], off offset:2112
	global_load_ushort v218, v[222:223], off offset:2304
	global_load_ushort v219, v[222:223], off offset:2368
	global_load_dwordx2 v[220:221], v[224:225], off
	s_branch .LBB0_585
; __device__ __forceinline__ float bf2f(bf16_t b) { return __uint_as_float((unsigned)b << 16); }
; __device__ __forceinline__ bf16_t f2bf(float f) { return (bf16_t)(cvt_pk_bf16(f, 0.f) & 0xffffu); }
; __device__ __forceinline__ void rope_token(const bf16_t* __restrict__ proj, const float* __restrict__ qg, const float* __restrict__ kg, bf16_t* __restrict__ QN, bf16_t* __restrict__ KN, bf16_t* __restrict__ VN, int tok, int lane) {
;     const int a = lane >> 5, f = lane & 31, i1 = a * 64 + f, i2 = i1 + 32; const int t = tok & (SEQ - 1);
;     const float pos = a == 0 ? (float)((t >> 6) - 32) : (float)((t & 63) - 32);
;     const float inv = exp2f(-(float)f * (13.287712379549449f / 32.f)); float sn, cs; sincosf(pos * inv, &sn, &cs);
;     const bf16_t* src = proj + (size_t)tok * NIN;
; #pragma unroll
;     for (int hh = 0; hh < 10; ++hh) { const bf16_t* s = src + hh * 128; float x1 = bf2f(s[i1]), x2 = bf2f(s[i2]);
;         const float ss = wave_sum(x1 * x1 + x2 * x2), rs = rsqrtf(ss * (1.f / 128.f) + EPS); const float* gn = hh < 8 ? qg : kg;
;         x1 *= rs * gn[i1]; x2 *= rs * gn[i2];
;         bf16_t* d = hh < 8 ? QN + (size_t)tok * 1024 + hh * 128 : KN + (size_t)tok * 256 + (hh - 8) * 128;
;         d[i1] = f2bf(x1 * cs - x2 * sn); d[i2] = f2bf(x2 * cs + x1 * sn); }
;     *(u32x2*)(VN + (size_t)tok * 256 + lane * 4) = *(const u32x2*)(src + C_V + lane * 4);
; }
.LBB0_584:
	s_or_b64 exec, exec, s[0:1]
	v_lshl_add_u64 v[16:17], s[52:53], 0, v[12:13]
	v_add_co_u32_e64 v16, s[0:1], s43, v16
	v_mul_f32_e32 v40, v2, v2
	s_nop 0
	v_addc_co_u32_e64 v17, s[0:1], 0, v17, s[0:1]
	s_nop 0
	s_nop 0
	v_lshlrev_b32_e32 v41, 30, v19
	v_and_b32_e32 v42, 1, v19
	v_xor_b32_e32 v43, v18, v35
	v_lshl_add_u64 v[18:19], s[52:53], 0, v[6:7]
	v_fmamk_f32 v44, v40, 0xb94c1982, v30
	v_fmamk_f32 v45, v40, 0x37d75334, v31
	v_add_co_u32_e64 v18, s[0:1], s44, v18
	v_fmaak_f32 v44, v40, v44, 0xbe2aaa9d
	v_fmaak_f32 v45, v40, v45, 0x3d2aabf7
	v_addc_co_u32_e64 v19, s[0:1], 0, v19, s[0:1]
	v_mul_f32_e32 v44, v40, v44
	v_fmaak_f32 v45, v40, v45, 0xbf000004
	v_fmac_f32_e32 v2, v2, v44
	v_fma_f32 v40, v40, v45, 1.0
	v_cmp_eq_u32_e64 s[0:1], 0, v42
	v_and_b32_e32 v46, 0x80000000, v41
	v_cmp_class_f32_e64 s[4:5], v35, s42
	v_cndmask_b32_e64 v42, v40, v2, s[0:1]
	v_xor_b32_e32 v2, 0x80000000, v2
	v_cndmask_b32_e64 v2, v2, v40, s[0:1]
	v_xor_b32_e32 v42, v43, v42
	v_xor_b32_e32 v40, v42, v46
	v_bitop3_b32 v2, v2, v41, s41 bitop3:0x78
	v_cndmask_b32_e64 v35, v34, v40, s[4:5]
	v_cndmask_b32_e64 v2, v34, v2, s[4:5]
	s_add_i32 s46, s46, s58
	v_lshl_add_u64 v[6:7], v[6:7], 0, s[14:15]
	s_cmpk_gt_i32 s46, 0x1fff
	v_lshl_add_u64 v[12:13], v[12:13], 0, s[22:23]
	v_lshl_add_u64 v[226:227], s[52:53], 0, v[10:11]
	v_lshl_add_u64 v[228:229], s[52:53], 0, v[8:9]
	v_add_co_u32_e64 v228, s[4:5], s45, v228
	v_lshl_add_u64 v[10:11], v[10:11], 0, s[16:17]
	v_lshl_add_u64 v[8:9], v[8:9], 0, s[16:17]
	v_addc_co_u32_e64 v229, s[4:5], 0, v229, s[4:5]
	v_lshl_add_u64 v[14:15], v[14:15], 0, s[22:23]
	s_waitcnt vmcnt(0)
	global_store_dwordx2 v[226:227], v[220:221], off
	v_lshlrev_b32_e32 v160, 16, v200
	v_lshlrev_b32_e32 v161, 16, v201
	v_lshlrev_b32_e32 v162, 16, v202
	v_lshlrev_b32_e32 v163, 16, v203
	v_lshlrev_b32_e32 v164, 16, v204
	v_lshlrev_b32_e32 v165, 16, v205
	v_lshlrev_b32_e32 v166, 16, v206
	v_lshlrev_b32_e32 v167, 16, v207
	v_lshlrev_b32_e32 v168, 16, v208
	v_lshlrev_b32_e32 v169, 16, v209
	v_lshlrev_b32_e32 v170, 16, v210
	v_lshlrev_b32_e32 v171, 16, v211
	v_lshlrev_b32_e32 v172, 16, v212
	v_lshlrev_b32_e32 v173, 16, v213
	v_lshlrev_b32_e32 v174, 16, v214
	v_lshlrev_b32_e32 v175, 16, v215
	v_lshlrev_b32_e32 v176, 16, v216
	v_lshlrev_b32_e32 v177, 16, v217
	v_lshlrev_b32_e32 v178, 16, v218
	v_lshlrev_b32_e32 v179, 16, v219
	s_cbranch_scc1 .Lrope_np_a
	v_lshl_add_u64 v[222:223], s[52:53], 0, v[12:13]
	v_lshl_add_u64 v[224:225], s[52:53], 0, v[14:15]
	v_add_co_u32_e64 v222, s[4:5], s43, v222
	s_nop 1
	v_addc_co_u32_e64 v223, s[4:5], 0, v223, s[4:5]
	global_load_ushort v200, v[222:223], off
	global_load_ushort v201, v[222:223], off offset:64
	global_load_ushort v202, v[222:223], off offset:256
	global_load_ushort v203, v[222:223], off offset:320
	global_load_ushort v204, v[222:223], off offset:512
	global_load_ushort v205, v[222:223], off offset:576
	global_load_ushort v206, v[222:223], off offset:768
	global_load_ushort v207, v[222:223], off offset:832
	global_load_ushort v208, v[222:223], off offset:1024
	global_load_ushort v209, v[222:223], off offset:1088
	global_load_ushort v210, v[222:223], off offset:1280
	global_load_ushort v211, v[222:223], off offset:1344
	global_load_ushort v212, v[222:223], off offset:1536
	global_load_ushort v213, v[222:223], off offset:1600
	global_load_ushort v214, v[222:223], off offset:1792
	global_load_ushort v215, v[222:223], off offset:1856
	global_load_ushort v216, v[222:223], off offset:2048
	global_load_ushort v217, v[222:223], off offset:2112
	global_load_ushort v218, v[222:223], off offset:2304
	global_load_ushort v219, v[222:223], off offset:2368
	global_load_dwordx2 v[220:221], v[224:225], off
.Lrope_np_a:
	v_pk_mul_f32 v[230:231], v[160:161], v[160:161]
	v_pk_mul_f32 v[232:233], v[162:163], v[162:163]
	v_pk_mul_f32 v[234:235], v[164:165], v[164:165]
	v_pk_mul_f32 v[236:237], v[166:167], v[166:167]
	v_pk_mul_f32 v[238:239], v[168:169], v[168:169]
	v_pk_mul_f32 v[240:241], v[170:171], v[170:171]
	v_pk_mul_f32 v[242:243], v[172:173], v[172:173]
	v_pk_mul_f32 v[244:245], v[174:175], v[174:175]
	v_pk_mul_f32 v[248:249], v[176:177], v[176:177]
	v_pk_mul_f32 v[250:251], v[178:179], v[178:179]
	v_add_f32_e32 v180, v230, v231
	v_add_f32_e32 v181, v232, v233
	v_add_f32_e32 v182, v234, v235
	v_add_f32_e32 v183, v236, v237
	v_add_f32_e32 v184, v238, v239
	v_add_f32_e32 v185, v240, v241
	v_add_f32_e32 v186, v242, v243
	v_add_f32_e32 v187, v244, v245
	v_add_f32_e32 v188, v248, v249
	v_add_f32_e32 v189, v250, v251
	v_add_f32_dpp v180, v180, v180 quad_perm:[1,0,3,2] row_mask:0xf bank_mask:0xf
	v_add_f32_dpp v181, v181, v181 quad_perm:[1,0,3,2] row_mask:0xf bank_mask:0xf
	v_add_f32_dpp v182, v182, v182 quad_perm:[1,0,3,2] row_mask:0xf bank_mask:0xf
	v_add_f32_dpp v183, v183, v183 quad_perm:[1,0,3,2] row_mask:0xf bank_mask:0xf
	v_add_f32_dpp v184, v184, v184 quad_perm:[1,0,3,2] row_mask:0xf bank_mask:0xf
	v_add_f32_dpp v185, v185, v185 quad_perm:[1,0,3,2] row_mask:0xf bank_mask:0xf
	v_add_f32_dpp v186, v186, v186 quad_perm:[1,0,3,2] row_mask:0xf bank_mask:0xf
	v_add_f32_dpp v187, v187, v187 quad_perm:[1,0,3,2] row_mask:0xf bank_mask:0xf
	v_add_f32_dpp v188, v188, v188 quad_perm:[1,0,3,2] row_mask:0xf bank_mask:0xf
	v_add_f32_dpp v189, v189, v189 quad_perm:[1,0,3,2] row_mask:0xf bank_mask:0xf
	v_add_f32_dpp v180, v180, v180 quad_perm:[2,3,0,1] row_mask:0xf bank_mask:0xf
	v_add_f32_dpp v181, v181, v181 quad_perm:[2,3,0,1] row_mask:0xf bank_mask:0xf
	v_add_f32_dpp v182, v182, v182 quad_perm:[2,3,0,1] row_mask:0xf bank_mask:0xf
	v_add_f32_dpp v183, v183, v183 quad_perm:[2,3,0,1] row_mask:0xf bank_mask:0xf
; __device__ __forceinline__ float bf2f(bf16_t b) { return __uint_as_float((unsigned)b << 16); }
; __device__ __forceinline__ bf16_t f2bf(float f) { return (bf16_t)(cvt_pk_bf16(f, 0.f) & 0xffffu); }
; __device__ __forceinline__ void rope_token(const bf16_t* __restrict__ proj, const float* __restrict__ qg, const float* __restrict__ kg, bf16_t* __restrict__ QN, bf16_t* __restrict__ KN, bf16_t* __restrict__ VN, int tok, int lane) {
;     const int a = lane >> 5, f = lane & 31, i1 = a * 64 + f, i2 = i1 + 32; const int t = tok & (SEQ - 1);
;     const float pos = a == 0 ? (float)((t >> 6) - 32) : (float)((t & 63) - 32);
;     const float inv = exp2f(-(float)f * (13.287712379549449f / 32.f)); float sn, cs; sincosf(pos * inv, &sn, &cs);
;     const bf16_t* src = proj + (size_t)tok * NIN;
; #pragma unroll
;     for (int hh = 0; hh < 10; ++hh) { const bf16_t* s = src + hh * 128; float x1 = bf2f(s[i1]), x2 = bf2f(s[i2]);
;         const float ss = wave_sum(x1 * x1 + x2 * x2), rs = rsqrtf(ss * (1.f / 128.f) + EPS); const float* gn = hh < 8 ? qg : kg;
;         x1 *= rs * gn[i1]; x2 *= rs * gn[i2];
;         bf16_t* d = hh < 8 ? QN + (size_t)tok * 1024 + hh * 128 : KN + (size_t)tok * 256 + (hh - 8) * 128;
;         d[i1] = f2bf(x1 * cs - x2 * sn); d[i2] = f2bf(x2 * cs + x1 * sn); }
;     *(u32x2*)(VN + (size_t)tok * 256 + lane * 4) = *(const u32x2*)(src + C_V + lane * 4);
; }
	v_add_f32_dpp v184, v184, v184 quad_perm:[2,3,0,1] row_mask:0xf bank_mask:0xf
	v_add_f32_dpp v185, v185, v185 quad_perm:[2,3,0,1] row_mask:0xf bank_mask:0xf
	v_add_f32_dpp v186, v186, v186 quad_perm:[2,3,0,1] row_mask:0xf bank_mask:0xf
	v_add_f32_dpp v187, v187, v187 quad_perm:[2,3,0,1] row_mask:0xf bank_mask:0xf
	v_add_f32_dpp v188, v188, v188 quad_perm:[2,3,0,1] row_mask:0xf bank_mask:0xf
	v_add_f32_dpp v189, v189, v189 quad_perm:[2,3,0,1] row_mask:0xf bank_mask:0xf
	v_add_f32_dpp v180, v180, v180 row_half_mirror row_mask:0xf bank_mask:0xf
	v_add_f32_dpp v181, v181, v181 row_half_mirror row_mask:0xf bank_mask:0xf
	v_add_f32_dpp v182, v182, v182 row_half_mirror row_mask:0xf bank_mask:0xf
	v_add_f32_dpp v183, v183, v183 row_half_mirror row_mask:0xf bank_mask:0xf
	v_add_f32_dpp v184, v184, v184 row_half_mirror row_mask:0xf bank_mask:0xf
	v_add_f32_dpp v185, v185, v185 row_half_mirror row_mask:0xf bank_mask:0xf
	v_add_f32_dpp v186, v186, v186 row_half_mirror row_mask:0xf bank_mask:0xf
	v_add_f32_dpp v187, v187, v187 row_half_mirror row_mask:0xf bank_mask:0xf
	v_add_f32_dpp v188, v188, v188 row_half_mirror row_mask:0xf bank_mask:0xf
	v_add_f32_dpp v189, v189, v189 row_half_mirror row_mask:0xf bank_mask:0xf
	v_add_f32_dpp v180, v180, v180 row_mirror row_mask:0xf bank_mask:0xf
	v_add_f32_dpp v181, v181, v181 row_mirror row_mask:0xf bank_mask:0xf
	v_add_f32_dpp v182, v182, v182 row_mirror row_mask:0xf bank_mask:0xf
	v_add_f32_dpp v183, v183, v183 row_mirror row_mask:0xf bank_mask:0xf
	v_add_f32_dpp v184, v184, v184 row_mirror row_mask:0xf bank_mask:0xf
	v_add_f32_dpp v185, v185, v185 row_mirror row_mask:0xf bank_mask:0xf
	v_add_f32_dpp v186, v186, v186 row_mirror row_mask:0xf bank_mask:0xf
	v_add_f32_dpp v187, v187, v187 row_mirror row_mask:0xf bank_mask:0xf
	v_add_f32_dpp v188, v188, v188 row_mirror row_mask:0xf bank_mask:0xf
	v_add_f32_dpp v189, v189, v189 row_mirror row_mask:0xf bank_mask:0xf
	v_add_f32_dpp v180, v180, v180 row_bcast:15 row_mask:0xa bank_mask:0xf
	v_add_f32_dpp v181, v181, v181 row_bcast:15 row_mask:0xa bank_mask:0xf
	v_add_f32_dpp v182, v182, v182 row_bcast:15 row_mask:0xa bank_mask:0xf
	v_add_f32_dpp v183, v183, v183 row_bcast:15 row_mask:0xa bank_mask:0xf
	v_add_f32_dpp v184, v184, v184 row_bcast:15 row_mask:0xa bank_mask:0xf
	v_add_f32_dpp v185, v185, v185 row_bcast:15 row_mask:0xa bank_mask:0xf
	v_add_f32_dpp v186, v186, v186 row_bcast:15 row_mask:0xa bank_mask:0xf
	v_add_f32_dpp v187, v187, v187 row_bcast:15 row_mask:0xa bank_mask:0xf
	v_add_f32_dpp v188, v188, v188 row_bcast:15 row_mask:0xa bank_mask:0xf
	v_add_f32_dpp v189, v189, v189 row_bcast:15 row_mask:0xa bank_mask:0xf
	v_add_f32_dpp v180, v180, v180 row_bcast:31 row_mask:0xc bank_mask:0xf
	v_add_f32_dpp v181, v181, v181 row_bcast:31 row_mask:0xc bank_mask:0xf
	v_add_f32_dpp v182, v182, v182 row_bcast:31 row_mask:0xc bank_mask:0xf
	v_add_f32_dpp v183, v183, v183 row_bcast:31 row_mask:0xc bank_mask:0xf
	v_add_f32_dpp v184, v184, v184 row_bcast:31 row_mask:0xc bank_mask:0xf
	v_add_f32_dpp v185, v185, v185 row_bcast:31 row_mask:0xc bank_mask:0xf
	v_add_f32_dpp v186, v186, v186 row_bcast:31 row_mask:0xc bank_mask:0xf
	v_add_f32_dpp v187, v187, v187 row_bcast:31 row_mask:0xc bank_mask:0xf
	v_add_f32_dpp v188, v188, v188 row_bcast:31 row_mask:0xc bank_mask:0xf
	v_add_f32_dpp v189, v189, v189 row_bcast:31 row_mask:0xc bank_mask:0xf
	v_readlane_b32 s4, v180, 63
	v_readlane_b32 s5, v181, 63
	v_readlane_b32 s6, v182, 63
	v_readlane_b32 s7, v183, 63
	v_readlane_b32 s8, v184, 63
	v_fma_f32 v180, s4, v192, v32
	v_fma_f32 v181, s5, v192, v32
	v_fma_f32 v182, s6, v192, v32
	v_fma_f32 v183, s7, v192, v32
	v_fma_f32 v184, s8, v192, v32
	v_rsq_f32_e32 v180, v180
	v_rsq_f32_e32 v181, v181
	v_rsq_f32_e32 v182, v182
	v_rsq_f32_e32 v183, v183
	v_rsq_f32_e32 v184, v184
	v_mul_f32_e32 v230, v22, v180
	v_mul_f32_e32 v231, v23, v180
	v_mul_f32_e32 v232, v230, v160
	v_mul_f32_e32 v233, v231, v161
	v_mul_f32_e32 v234, v35, v233
	v_mul_f32_e32 v235, v35, v232
	v_fma_f32 v236, v2, v232, -v234
	v_fmac_f32_e32 v235, v2, v233
	v_cvt_pk_bf16_f32 v236, v236, v3
	v_cvt_pk_bf16_f32 v235, v235, v3
	global_store_short v[18:19], v236, off
	global_store_short v[18:19], v235, off offset:64
	v_mul_f32_e32 v238, v22, v181
; __device__ __forceinline__ float bf2f(bf16_t b) { return __uint_as_float((unsigned)b << 16); }
; __device__ __forceinline__ bf16_t f2bf(float f) { return (bf16_t)(cvt_pk_bf16(f, 0.f) & 0xffffu); }
; __device__ __forceinline__ void rope_token(const bf16_t* __restrict__ proj, const float* __restrict__ qg, const float* __restrict__ kg, bf16_t* __restrict__ QN, bf16_t* __restrict__ KN, bf16_t* __restrict__ VN, int tok, int lane) {
;     const int a = lane >> 5, f = lane & 31, i1 = a * 64 + f, i2 = i1 + 32; const int t = tok & (SEQ - 1);
;     const float pos = a == 0 ? (float)((t >> 6) - 32) : (float)((t & 63) - 32);
;     const float inv = exp2f(-(float)f * (13.287712379549449f / 32.f)); float sn, cs; sincosf(pos * inv, &sn, &cs);
;     const bf16_t* src = proj + (size_t)tok * NIN;
; #pragma unroll
;     for (int hh = 0; hh < 10; ++hh) { const bf16_t* s = src + hh * 128; float x1 = bf2f(s[i1]), x2 = bf2f(s[i2]);
;         const float ss = wave_sum(x1 * x1 + x2 * x2), rs = rsqrtf(ss * (1.f / 128.f) + EPS); const float* gn = hh < 8 ? qg : kg;
;         x1 *= rs * gn[i1]; x2 *= rs * gn[i2];
;         bf16_t* d = hh < 8 ? QN + (size_t)tok * 1024 + hh * 128 : KN + (size_t)tok * 256 + (hh - 8) * 128;
;         d[i1] = f2bf(x1 * cs - x2 * sn); d[i2] = f2bf(x2 * cs + x1 * sn); }
;     *(u32x2*)(VN + (size_t)tok * 256 + lane * 4) = *(const u32x2*)(src + C_V + lane * 4);
; }
	v_mul_f32_e32 v239, v23, v181
	v_mul_f32_e32 v240, v238, v162
	v_mul_f32_e32 v241, v239, v163
	v_mul_f32_e32 v242, v35, v241
	v_mul_f32_e32 v243, v35, v240
	v_fma_f32 v244, v2, v240, -v242
	v_fmac_f32_e32 v243, v2, v241
	v_cvt_pk_bf16_f32 v244, v244, v3
	v_cvt_pk_bf16_f32 v243, v243, v3
	global_store_short v[18:19], v244, off offset:256
	global_store_short v[18:19], v243, off offset:320
	v_mul_f32_e32 v230, v22, v182
	v_mul_f32_e32 v231, v23, v182
	v_mul_f32_e32 v232, v230, v164
	v_mul_f32_e32 v233, v231, v165
	v_mul_f32_e32 v234, v35, v233
	v_mul_f32_e32 v235, v35, v232
	v_fma_f32 v236, v2, v232, -v234
	v_fmac_f32_e32 v235, v2, v233
	v_cvt_pk_bf16_f32 v236, v236, v3
	v_cvt_pk_bf16_f32 v235, v235, v3
	global_store_short v[18:19], v236, off offset:512
	global_store_short v[18:19], v235, off offset:576
	v_mul_f32_e32 v238, v22, v183
	v_mul_f32_e32 v239, v23, v183
	v_mul_f32_e32 v240, v238, v166
	v_mul_f32_e32 v241, v239, v167
	v_mul_f32_e32 v242, v35, v241
	v_mul_f32_e32 v243, v35, v240
	v_fma_f32 v244, v2, v240, -v242
	v_fmac_f32_e32 v243, v2, v241
	v_cvt_pk_bf16_f32 v244, v244, v3
	v_cvt_pk_bf16_f32 v243, v243, v3
	global_store_short v[18:19], v244, off offset:768
	global_store_short v[18:19], v243, off offset:832
	v_mul_f32_e32 v230, v22, v184
	v_mul_f32_e32 v231, v23, v184
	v_mul_f32_e32 v232, v230, v168
	v_mul_f32_e32 v233, v231, v169
	v_mul_f32_e32 v234, v35, v233
	v_mul_f32_e32 v235, v35, v232
	v_fma_f32 v236, v2, v232, -v234
	v_fmac_f32_e32 v235, v2, v233
	v_cvt_pk_bf16_f32 v236, v236, v3
	v_cvt_pk_bf16_f32 v235, v235, v3
	global_store_short v[18:19], v236, off offset:1024
	global_store_short v[18:19], v235, off offset:1088
	v_readlane_b32 s4, v185, 63
	v_readlane_b32 s5, v186, 63
	v_readlane_b32 s6, v187, 63
	v_readlane_b32 s7, v188, 63
	v_readlane_b32 s8, v189, 63
	v_fma_f32 v185, s4, v192, v32
	v_fma_f32 v186, s5, v192, v32
	v_fma_f32 v187, s6, v192, v32
	v_fma_f32 v188, s7, v192, v32
	v_fma_f32 v189, s8, v192, v32
	v_rsq_f32_e32 v185, v185
	v_rsq_f32_e32 v186, v186
	v_rsq_f32_e32 v187, v187
	v_rsq_f32_e32 v188, v188
	v_rsq_f32_e32 v189, v189
	v_mul_f32_e32 v238, v22, v185
	v_mul_f32_e32 v239, v23, v185
	v_mul_f32_e32 v240, v238, v170
	v_mul_f32_e32 v241, v239, v171
	v_mul_f32_e32 v242, v35, v241
	v_mul_f32_e32 v243, v35, v240
	v_fma_f32 v244, v2, v240, -v242
	v_fmac_f32_e32 v243, v2, v241
	v_cvt_pk_bf16_f32 v244, v244, v3
	v_cvt_pk_bf16_f32 v243, v243, v3
	global_store_short v[18:19], v244, off offset:1280
	global_store_short v[18:19], v243, off offset:1344
	v_mul_f32_e32 v230, v22, v186
	v_mul_f32_e32 v231, v23, v186
	v_mul_f32_e32 v232, v230, v172
	v_mul_f32_e32 v233, v231, v173
	v_mul_f32_e32 v234, v35, v233
	v_mul_f32_e32 v235, v35, v232
	v_fma_f32 v236, v2, v232, -v234
	v_fmac_f32_e32 v235, v2, v233
	v_cvt_pk_bf16_f32 v236, v236, v3
	v_cvt_pk_bf16_f32 v235, v235, v3
	global_store_short v[18:19], v236, off offset:1536
	global_store_short v[18:19], v235, off offset:1600
	v_mul_f32_e32 v238, v22, v187
	v_mul_f32_e32 v239, v23, v187
	v_mul_f32_e32 v240, v238, v174
	v_mul_f32_e32 v241, v239, v175
	v_mul_f32_e32 v242, v35, v241
	v_mul_f32_e32 v243, v35, v240
	v_fma_f32 v244, v2, v240, -v242
	v_fmac_f32_e32 v243, v2, v241
	v_cvt_pk_bf16_f32 v244, v244, v3
	v_cvt_pk_bf16_f32 v243, v243, v3
	global_store_short v[18:19], v244, off offset:1792
	global_store_short v[18:19], v243, off offset:1856
	v_mul_f32_e32 v230, v190, v188
	v_mul_f32_e32 v231, v191, v188
	v_mul_f32_e32 v232, v230, v176
	v_mul_f32_e32 v233, v231, v177
	v_mul_f32_e32 v234, v35, v233
	v_mul_f32_e32 v235, v35, v232
	v_fma_f32 v236, v2, v232, -v234
	v_fmac_f32_e32 v235, v2, v233
	v_cvt_pk_bf16_f32 v236, v236, v3
	v_cvt_pk_bf16_f32 v235, v235, v3
	global_store_short v[228:229], v236, off
	global_store_short v[228:229], v235, off offset:64
	v_mul_f32_e32 v238, v190, v189
	v_mul_f32_e32 v239, v191, v189
	v_mul_f32_e32 v240, v238, v178
	v_mul_f32_e32 v241, v239, v179
	v_mul_f32_e32 v242, v35, v241
	v_mul_f32_e32 v243, v35, v240
	v_fma_f32 v244, v2, v240, -v242
	v_fmac_f32_e32 v243, v2, v241
	v_cvt_pk_bf16_f32 v244, v244, v3
	v_cvt_pk_bf16_f32 v243, v243, v3
	global_store_short v[228:229], v244, off offset:256
	global_store_short v[228:229], v243, off offset:320
	s_cbranch_scc1 .LBB0_589

; __device__ __forceinline__ float bf2f(bf16_t b) { return __uint_as_float((unsigned)b << 16); }
; __device__ __forceinline__ bf16_t f2bf(float f) { return (bf16_t)(cvt_pk_bf16(f, 0.f) & 0xffffu); }
; __device__ __forceinline__ void rope_token(const bf16_t* __restrict__ proj, const float* __restrict__ qg, const float* __restrict__ kg, bf16_t* __restrict__ QN, bf16_t* __restrict__ KN, bf16_t* __restrict__ VN, int tok, int lane) {
;     const int a = lane >> 5, f = lane & 31, i1 = a * 64 + f, i2 = i1 + 32; const int t = tok & (SEQ - 1);
;     const float pos = a == 0 ? (float)((t >> 6) - 32) : (float)((t & 63) - 32);
;     const float inv = exp2f(-(float)f * (13.287712379549449f / 32.f)); float sn, cs; sincosf(pos * inv, &sn, &cs);
;     const bf16_t* src = proj + (size_t)tok * NIN;
; #pragma unroll
;     for (int hh = 0; hh < 10; ++hh) { const bf16_t* s = src + hh * 128; float x1 = bf2f(s[i1]), x2 = bf2f(s[i2]);
;         const float ss = wave_sum(x1 * x1 + x2 * x2), rs = rsqrtf(ss * (1.f / 128.f) + EPS); const float* gn = hh < 8 ? qg : kg;
;         x1 *= rs * gn[i1]; x2 *= rs * gn[i2];
;         bf16_t* d = hh < 8 ? QN + (size_t)tok * 1024 + hh * 128 : KN + (size_t)tok * 256 + (hh - 8) * 128;
;         d[i1] = f2bf(x1 * cs - x2 * sn); d[i2] = f2bf(x2 * cs + x1 * sn); }
;     *(u32x2*)(VN + (size_t)tok * 256 + lane * 4) = *(const u32x2*)(src + C_V + lane * 4);
; }
; __global__ void __launch_bounds__(NWAVES * 64, 2) mk_fwd(Args a) {
;     ...
;         { for (int tok = gw; tok < NT; tok += ngw) thin::rope_token(PROJ, a.in[4] + l * 128, a.in[5] + l * 128, QN, KN, VN, tok, lane);
.LBB0_1560:
	s_cmpk_gt_i32 s96, 0x1fff
	s_cbranch_scc1 .LBB0_1573
	v_and_b32_e32 v133, 31, v0
	s_waitcnt vmcnt(0)
	v_cvt_f32_ubyte0_e32 v2, v133
	s_waitcnt lgkmcnt(0)
	v_mul_f32_e32 v3, 0xbed49a78, v2
	s_mov_b32 s0, 0xc2fc0000
	v_mov_b32_e32 v4, 0x42800000
	v_cmp_gt_f32_e64 s[0:1], s0, v3
	v_not_b32_e32 v20, 63
	v_readlane_b32 s36, v247, 3
	v_cndmask_b32_e64 v3, 0, v4, s[0:1]
	v_fmac_f32_e32 v3, 0xbed49a78, v2
	v_exp_f32_e32 v2, v3
	v_cndmask_b32_e64 v3, 0, v20, s[0:1]
	v_readlane_b32 s44, v247, 11
	v_readlane_b32 s45, v247, 12
	v_ldexp_f32 v21, v2, v3
	v_lshlrev_b32_e32 v2, 1, v0
	v_and_or_b32 v6, v2, 64, v133
	v_lshlrev_b32_e32 v2, 2, v6
	v_readlane_b32 s46, v247, 13
	v_readlane_b32 s47, v247, 14
	s_mov_b64 s[20:21], s[44:45]
	global_load_dword v22, v2, s[20:21] offset:512
	global_load_dword v23, v2, s[20:21] offset:640
	v_mbcnt_lo_u32_b32 v3, -1, 0
	v_mbcnt_hi_u32_b32 v3, -1, v3
	v_and_b32_e32 v4, 64, v3
	v_add_u32_e32 v4, 64, v4
	v_xor_b32_e32 v5, 1, v3
	v_cmp_lt_i32_e64 s[0:1], v5, v4
	s_mov_b64 s[22:23], s[46:47]
	s_ashr_i32 s97, s96, 31
	v_cndmask_b32_e64 v5, v3, v5, s[0:1]
	v_lshlrev_b32_e32 v24, 2, v5
	v_xor_b32_e32 v5, 2, v3
	v_cmp_lt_i32_e64 s[0:1], v5, v4
	v_lshlrev_b32_e32 v12, 3, v194
	s_mul_i32 s3, s96, 0x5400
	v_cndmask_b32_e64 v5, v3, v5, s[0:1]
	v_lshlrev_b32_e32 v25, 2, v5
	v_xor_b32_e32 v5, 4, v3
	v_cmp_lt_i32_e64 s[0:1], v5, v4
	v_readlane_b32 s37, v247, 4
	v_readlane_b32 s38, v247, 5
	v_cndmask_b32_e64 v5, v3, v5, s[0:1]
	v_lshlrev_b32_e32 v26, 2, v5
	v_xor_b32_e32 v5, 8, v3
	v_cmp_lt_i32_e64 s[0:1], v5, v4
	v_readlane_b32 s39, v247, 6
	v_readlane_b32 s50, v247, 17
	v_cndmask_b32_e64 v5, v3, v5, s[0:1]
	v_lshlrev_b32_e32 v27, 2, v5
	v_xor_b32_e32 v5, 16, v3
	v_cmp_lt_i32_e64 s[0:1], v5, v4
	v_readlane_b32 s51, v247, 18
	s_ashr_i32 s59, s58, 31
	v_cndmask_b32_e64 v5, v3, v5, s[0:1]
	v_lshlrev_b32_e32 v28, 2, v5
	v_xor_b32_e32 v5, 32, v3
	v_cmp_lt_i32_e64 s[0:1], v5, v4
	v_cmp_gt_u32_e32 vcc, 32, v194
	s_lshl_b64 s[14:15], s[58:59], 11
	v_cndmask_b32_e64 v3, v3, v5, s[0:1]
	v_lshlrev_b32_e32 v29, 2, v3
	v_mov_b32_e32 v3, 0
	v_lshl_add_u64 v[4:5], s[22:23], 0, v[2:3]
	s_lshl_b64 s[0:1], s[96:97], 11
	v_lshlrev_b32_e32 v2, 1, v6
	v_or_b32_e32 v6, s0, v2
	v_mov_b32_e32 v7, s1
	s_lshl_b64 s[0:1], s[96:97], 9
	v_or_b32_e32 v8, s0, v2
	v_mov_b32_e32 v9, s1
	v_or_b32_e32 v10, s0, v12
	v_mov_b32_e32 v11, s1
	s_mov_b64 s[0:1], 0x4e200000
	v_lshl_add_u64 v[10:11], v[10:11], 0, s[0:1]
	s_mul_hi_i32 s0, s96, 0x5400
	v_or_b32_e32 v12, s3, v12
	v_mov_b32_e32 v13, s0
	s_mov_b64 s[0:1], 0x42600a00
	s_lshl_b64 s[16:17], s[58:59], 9
	v_lshl_add_u64 v[14:15], v[12:13], 0, s[0:1]
	s_mul_hi_i32 s39, s58, 0x5400
	s_mul_i32 s38, s58, 0x5400
	v_or_b32_e32 v12, s3, v2
	s_brev_b32 s3, 18
	s_mov_b32 s20, 0x800000
	s_mov_b32 s21, 0xfe5163ab
	s_mov_b32 s22, 0x3c439041
	s_mov_b32 s23, 0xdb629599
	s_mov_b32 s34, 0xf534ddc0
	s_mov_b32 s35, 0xfc2757d1
	s_mov_b32 s36, 0x4e441529
	s_mov_b32 s37, 0xa2f9836e
	s_mov_b32 s44, 0x3fc90fda
	s_mov_b32 s45, 0x3f22f983
	s_mov_b32 s50, 0xbfc90fda
	v_mov_b32_e32 v30, 0x3c0881c4
	v_mov_b32_e32 v31, 0xbab64f3b
	s_brev_b32 s51, 1
	s_movk_i32 s56, 0x1f8
	s_mov_b32 s57, 0x42600000
	v_mov_b32_e32 v32, 0x358637bd
	s_mov_b32 s59, 0x4ce00000
	s_mov_b32 s66, 0x4de00000
	v_not_b32_e32 v33, 31
	v_mov_b32_e32 v34, 0x7fc00000
	s_mov_b32 s67, s96
	v_readlane_b32 s40, v247, 7
	v_readlane_b32 s41, v247, 8
	v_readlane_b32 s42, v247, 9
	v_readlane_b32 s43, v247, 10
	v_readlane_b32 s48, v247, 15
	v_readlane_b32 s49, v247, 16
	v_lshl_add_u64 v[222:223], s[52:53], 0, v[12:13]
	v_lshl_add_u64 v[224:225], s[52:53], 0, v[14:15]
	v_mov_b32_e32 v192, 0x3c000000
	v_add_co_u32_e64 v222, s[0:1], s57, v222
	s_nop 1
	v_addc_co_u32_e64 v223, s[0:1], 0, v223, s[0:1]
	global_load_dword v190, v[4:5], off offset:512
	global_load_dword v191, v[4:5], off offset:640
	global_load_ushort v200, v[222:223], off
	global_load_ushort v201, v[222:223], off offset:64
	global_load_ushort v202, v[222:223], off offset:256
	global_load_ushort v203, v[222:223], off offset:320
	global_load_ushort v204, v[222:223], off offset:512
	global_load_ushort v205, v[222:223], off offset:576
	global_load_ushort v206, v[222:223], off offset:768
	global_load_ushort v207, v[222:223], off offset:832
	global_load_ushort v208, v[222:223], off offset:1024
	global_load_ushort v209, v[222:223], off offset:1088
	global_load_ushort v210, v[222:223], off offset:1280
	global_load_ushort v211, v[222:223], off offset:1344
	global_load_ushort v212, v[222:223], off offset:1536
	global_load_ushort v213, v[222:223], off offset:1600
	global_load_ushort v214, v[222:223], off offset:1792
	global_load_ushort v215, v[222:223], off offset:1856
	global_load_ushort v216, v[222:223], off offset:2048
	global_load_ushort v217, v[222:223], off offset:2112
	global_load_ushort v218, v[222:223], off offset:2304
	global_load_ushort v219, v[222:223], off offset:2368
	global_load_dwordx2 v[220:221], v[224:225], off
	s_branch .LBB0_1563
; __device__ __forceinline__ float bf2f(bf16_t b) { return __uint_as_float((unsigned)b << 16); }
; __device__ __forceinline__ bf16_t f2bf(float f) { return (bf16_t)(cvt_pk_bf16(f, 0.f) & 0xffffu); }
; __device__ __forceinline__ void rope_token(const bf16_t* __restrict__ proj, const float* __restrict__ qg, const float* __restrict__ kg, bf16_t* __restrict__ QN, bf16_t* __restrict__ KN, bf16_t* __restrict__ VN, int tok, int lane) {
;     const int a = lane >> 5, f = lane & 31, i1 = a * 64 + f, i2 = i1 + 32; const int t = tok & (SEQ - 1);
;     const float pos = a == 0 ? (float)((t >> 6) - 32) : (float)((t & 63) - 32);
;     const float inv = exp2f(-(float)f * (13.287712379549449f / 32.f)); float sn, cs; sincosf(pos * inv, &sn, &cs);
;     const bf16_t* src = proj + (size_t)tok * NIN;
; #pragma unroll
;     for (int hh = 0; hh < 10; ++hh) { const bf16_t* s = src + hh * 128; float x1 = bf2f(s[i1]), x2 = bf2f(s[i2]);
;         const float ss = wave_sum(x1 * x1 + x2 * x2), rs = rsqrtf(ss * (1.f / 128.f) + EPS); const float* gn = hh < 8 ? qg : kg;
;         x1 *= rs * gn[i1]; x2 *= rs * gn[i2];
;         bf16_t* d = hh < 8 ? QN + (size_t)tok * 1024 + hh * 128 : KN + (size_t)tok * 256 + (hh - 8) * 128;
;         d[i1] = f2bf(x1 * cs - x2 * sn); d[i2] = f2bf(x2 * cs + x1 * sn); }
;     *(u32x2*)(VN + (size_t)tok * 256 + lane * 4) = *(const u32x2*)(src + C_V + lane * 4);
; }
.LBB0_1562:
	s_or_b64 exec, exec, s[0:1]
	v_lshl_add_u64 v[16:17], s[52:53], 0, v[12:13]
	v_add_co_u32_e64 v16, s[0:1], s57, v16
	v_mul_f32_e32 v40, v2, v2
	s_nop 0
	v_addc_co_u32_e64 v17, s[0:1], 0, v17, s[0:1]
	s_nop 0
	s_nop 0
	v_lshlrev_b32_e32 v41, 30, v19
	v_and_b32_e32 v42, 1, v19
	v_xor_b32_e32 v43, v18, v35
	v_lshl_add_u64 v[18:19], s[52:53], 0, v[6:7]
	v_fmamk_f32 v44, v40, 0xb94c1982, v30
	v_fmamk_f32 v45, v40, 0x37d75334, v31
	v_add_co_u32_e64 v18, s[0:1], s59, v18
	v_fmaak_f32 v44, v40, v44, 0xbe2aaa9d
	v_fmaak_f32 v45, v40, v45, 0x3d2aabf7
	v_addc_co_u32_e64 v19, s[0:1], 0, v19, s[0:1]
	v_mul_f32_e32 v44, v40, v44
	v_fmaak_f32 v45, v40, v45, 0xbf000004
	v_fmac_f32_e32 v2, v2, v44
	v_fma_f32 v40, v40, v45, 1.0
	v_cmp_eq_u32_e64 s[0:1], 0, v42
	v_and_b32_e32 v46, 0x80000000, v41
	v_cmp_class_f32_e64 s[4:5], v35, s56
	v_cndmask_b32_e64 v42, v40, v2, s[0:1]
	v_xor_b32_e32 v2, 0x80000000, v2
	v_cndmask_b32_e64 v2, v2, v40, s[0:1]
	v_xor_b32_e32 v42, v43, v42
	v_xor_b32_e32 v40, v42, v46
	v_bitop3_b32 v2, v2, v41, s51 bitop3:0x78
	v_cndmask_b32_e64 v35, v34, v40, s[4:5]
	v_cndmask_b32_e64 v2, v34, v2, s[4:5]
	s_add_i32 s67, s67, s58
	v_lshl_add_u64 v[6:7], v[6:7], 0, s[14:15]
	s_cmpk_gt_i32 s67, 0x1fff
	v_lshl_add_u64 v[12:13], v[12:13], 0, s[38:39]
	v_lshl_add_u64 v[226:227], s[52:53], 0, v[10:11]
	v_lshl_add_u64 v[228:229], s[52:53], 0, v[8:9]
	v_add_co_u32_e64 v228, s[4:5], s66, v228
	v_lshl_add_u64 v[10:11], v[10:11], 0, s[16:17]
	v_lshl_add_u64 v[8:9], v[8:9], 0, s[16:17]
	v_addc_co_u32_e64 v229, s[4:5], 0, v229, s[4:5]
	v_lshl_add_u64 v[14:15], v[14:15], 0, s[38:39]
	s_waitcnt vmcnt(0)
	global_store_dwordx2 v[226:227], v[220:221], off
	v_lshlrev_b32_e32 v160, 16, v200
	v_lshlrev_b32_e32 v161, 16, v201
	v_lshlrev_b32_e32 v162, 16, v202
	v_lshlrev_b32_e32 v163, 16, v203
	v_lshlrev_b32_e32 v164, 16, v204
	v_lshlrev_b32_e32 v165, 16, v205
	v_lshlrev_b32_e32 v166, 16, v206
	v_lshlrev_b32_e32 v167, 16, v207
	v_lshlrev_b32_e32 v168, 16, v208
	v_lshlrev_b32_e32 v169, 16, v209
	v_lshlrev_b32_e32 v170, 16, v210
	v_lshlrev_b32_e32 v171, 16, v211
	v_lshlrev_b32_e32 v172, 16, v212
	v_lshlrev_b32_e32 v173, 16, v213
	v_lshlrev_b32_e32 v174, 16, v214
	v_lshlrev_b32_e32 v175, 16, v215
	v_lshlrev_b32_e32 v176, 16, v216
	v_lshlrev_b32_e32 v177, 16, v217
	v_lshlrev_b32_e32 v178, 16, v218
	v_lshlrev_b32_e32 v179, 16, v219
	s_cbranch_scc1 .Lrope_np_b
	v_lshl_add_u64 v[222:223], s[52:53], 0, v[12:13]
	v_lshl_add_u64 v[224:225], s[52:53], 0, v[14:15]
	v_add_co_u32_e64 v222, s[4:5], s57, v222
	s_nop 1
	v_addc_co_u32_e64 v223, s[4:5], 0, v223, s[4:5]
	global_load_ushort v200, v[222:223], off
	global_load_ushort v201, v[222:223], off offset:64
	global_load_ushort v202, v[222:223], off offset:256
	global_load_ushort v203, v[222:223], off offset:320
	global_load_ushort v204, v[222:223], off offset:512
	global_load_ushort v205, v[222:223], off offset:576
	global_load_ushort v206, v[222:223], off offset:768
	global_load_ushort v207, v[222:223], off offset:832
	global_load_ushort v208, v[222:223], off offset:1024
	global_load_ushort v209, v[222:223], off offset:1088
	global_load_ushort v210, v[222:223], off offset:1280
	global_load_ushort v211, v[222:223], off offset:1344
	global_load_ushort v212, v[222:223], off offset:1536
	global_load_ushort v213, v[222:223], off offset:1600
	global_load_ushort v214, v[222:223], off offset:1792
	global_load_ushort v215, v[222:223], off offset:1856
	global_load_ushort v216, v[222:223], off offset:2048
	global_load_ushort v217, v[222:223], off offset:2112
	global_load_ushort v218, v[222:223], off offset:2304
	global_load_ushort v219, v[222:223], off offset:2368
	global_load_dwordx2 v[220:221], v[224:225], off
